# P13 tile loop: K fragment ds_reads of d0=1..3 issued together with counted lgkmcnt waits (v240-v251), stacked on v015
# speedup vs baseline: 1.0032x; 1.0032x over previous
.LBB0_2751:
	ds_read_b64 v[226:227], v146
	v_add_u32_e32 v179, s39, v151
	v_add_u32_e32 v225, v179, v155
	v_add_u32_e32 v224, v179, v181
	v_add_u32_e32 v223, v179, v219
	s_waitcnt lgkmcnt(0)
	v_lshrrev_b32_e32 v82, v163, v226
	v_bfe_i32 v83, v82, 26, 1
	v_bitop3_b32 v96, v16, s28, v83 bitop3:0xe4
	v_bfe_i32 v83, v82, 25, 1
	v_bitop3_b32 v95, v13, s28, v83 bitop3:0xe4
	v_bfe_i32 v83, v82, 24, 1
	v_bitop3_b32 v94, v14, s28, v83 bitop3:0xe4
	v_bfe_i32 v83, v82, 19, 1
	v_bitop3_b32 v93, v11, s28, v83 bitop3:0xe4
	v_bfe_i32 v83, v82, 18, 1
	v_bitop3_b32 v92, v12, s28, v83 bitop3:0xe4
	v_bfe_i32 v83, v82, 17, 1
	v_add_u32_e32 v226, v179, v153
	v_bitop3_b32 v91, v9, s28, v83 bitop3:0xe4
	v_bfe_i32 v83, v82, 16, 1
	ds_read_b128 v[186:189], v226
	v_bitop3_b32 v90, v10, s28, v83 bitop3:0xe4
	v_bfe_i32 v83, v82, 11, 1
	v_bitop3_b32 v89, v7, s28, v83 bitop3:0xe4
	v_bfe_i32 v83, v82, 10, 1
	v_bitop3_b32 v88, v8, s28, v83 bitop3:0xe4
	v_bfe_i32 v83, v82, 9, 1
	v_bitop3_b32 v87, v5, s28, v83 bitop3:0xe4
	v_bfe_i32 v83, v82, 8, 1
	v_bitop3_b32 v86, v6, s28, v83 bitop3:0xe4
	v_bfe_i32 v83, v82, 3, 1
	v_bfe_i32 v84, v82, 27, 1
	v_bitop3_b32 v85, v3, s28, v83 bitop3:0xe4
	v_bfe_i32 v83, v82, 2, 1
	v_bitop3_b32 v97, v15, s28, v84 bitop3:0xe4
	v_bitop3_b32 v84, v4, s28, v83 bitop3:0xe4
	v_bfe_i32 v83, v82, 1, 1
	v_bfe_i32 v82, v82, 0, 1
	v_bitop3_b32 v83, v1, s28, v83 bitop3:0xe4
	v_bitop3_b32 v82, v2, s28, v82 bitop3:0xe4
	v_add_u32_e32 v179, s39, v17
	s_add_i32 s14, s37, 1
	ds_read_b128 v[240:243], v225
	ds_read_b128 v[244:247], v224
	ds_read_b128 v[248:251], v223
	s_waitcnt lgkmcnt(3)
	v_mfma_f32_32x32x16_bf16 v[98:113], v[186:189], v[114:117], v[82:97]
	s_cmp_lg_u32 s37, 2
	s_cselect_b32 s37, s14, 0
	s_add_u32 s0, s0, 0x4000
	s_addc_u32 s1, s1, 0
	s_add_i32 s38, s38, 1
	s_cmp_eq_u32 s36, s0
	v_add_u32_e32 v146, 8, v146
	v_mfma_f32_32x32x16_bf16 v[82:97], v[186:189], v[130:133], v[82:97]
	s_waitcnt lgkmcnt(2)
	v_mfma_f32_32x32x16_bf16 v[98:113], v[240:243], v[118:121], v[98:113]
	v_mfma_f32_32x32x16_bf16 v[82:97], v[240:243], v[134:137], v[82:97]
	s_waitcnt lgkmcnt(1)
	v_mfma_f32_32x32x16_bf16 v[98:113], v[244:247], v[122:125], v[98:113]
	v_mfma_f32_32x32x16_bf16 v[82:97], v[244:247], v[138:141], v[82:97]
	s_waitcnt lgkmcnt(0)
	v_mfma_f32_32x32x16_bf16 v[98:113], v[248:251], v[126:129], v[98:113]
	v_mfma_f32_32x32x16_bf16 v[82:97], v[248:251], v[142:145], v[82:97]
	s_nop 10
	v_exp_f32_e32 v190, v98
	v_exp_f32_e32 v191, v99
	v_exp_f32_e32 v192, v100
	v_exp_f32_e32 v193, v101
	s_waitcnt vmcnt(0)
	ds_read_b64_tr_b16 v[98:99], v179 offset:49152
	ds_read_b64_tr_b16 v[100:101], v179 offset:50176
	v_exp_f32_e32 v188, v102
	v_exp_f32_e32 v189, v103
	v_exp_f32_e32 v186, v104
	v_exp_f32_e32 v187, v105
	ds_read_b64_tr_b16 v[212:213], v179 offset:50688
	ds_read_b64_tr_b16 v[210:211], v179 offset:49664
	v_exp_f32_e32 v204, v82
	v_exp_f32_e32 v205, v83
	v_exp_f32_e32 v208, v84
	v_exp_f32_e32 v209, v85
	v_exp_f32_e32 v200, v86
	v_exp_f32_e32 v201, v87
	v_exp_f32_e32 v196, v88
	v_exp_f32_e32 v197, v89
	v_cvt_pk_bf16_f32 v102, v190, v191
	v_cvt_pk_bf16_f32 v103, v192, v193
	v_cvt_pk_bf16_f32 v104, v188, v189
	v_cvt_pk_bf16_f32 v105, v186, v187
	v_cvt_pk_bf16_f32 v82, v204, v205
	v_cvt_pk_bf16_f32 v83, v208, v209
	s_waitcnt lgkmcnt(2)
	v_mfma_f32_32x32x16_bf16 v[66:81], v[98:101], v[102:105], v[66:81]
	v_cvt_pk_bf16_f32 v84, v200, v201
	v_cvt_pk_bf16_f32 v85, v196, v197
	v_exp_f32_e32 v206, v106
	v_exp_f32_e32 v207, v107
	v_exp_f32_e32 v202, v108
	v_exp_f32_e32 v203, v109
	v_exp_f32_e32 v198, v110
	s_waitcnt lgkmcnt(0)
	v_mfma_f32_32x32x16_bf16 v[50:65], v[210:213], v[102:105], v[50:65]
	v_exp_f32_e32 v199, v111
	v_exp_f32_e32 v194, v112
	v_exp_f32_e32 v195, v113
	v_exp_f32_e32 v216, v90
	v_exp_f32_e32 v217, v91
	v_exp_f32_e32 v214, v92
	v_exp_f32_e32 v215, v93
	v_mfma_f32_32x32x16_bf16 v[34:49], v[98:101], v[82:85], v[34:49]
	v_cvt_pk_bf16_f32 v86, v206, v207
	v_cvt_pk_bf16_f32 v87, v202, v203
	v_cvt_pk_bf16_f32 v88, v198, v199
	v_cvt_pk_bf16_f32 v89, v194, v195
	v_mfma_f32_32x32x16_bf16 v[18:33], v[210:213], v[82:85], v[18:33]
	ds_read_b64_tr_b16 v[82:83], v179 offset:51200
	ds_read_b64_tr_b16 v[84:85], v179 offset:52224
	ds_read_b64_tr_b16 v[100:101], v179 offset:52736
	ds_read_b64_tr_b16 v[98:99], v179 offset:51712
	v_exp_f32_e32 v212, v94
	v_exp_f32_e32 v213, v95
	v_exp_f32_e32 v210, v96
	v_exp_f32_e32 v211, v97
	s_waitcnt lgkmcnt(2)
	v_mfma_f32_32x32x16_bf16 v[66:81], v[82:85], v[86:89], v[66:81]
	s_waitcnt lgkmcnt(0)
	v_mfma_f32_32x32x16_bf16 v[50:65], v[98:101], v[86:89], v[50:65]
	v_cvt_pk_bf16_f32 v86, v216, v217
	v_cvt_pk_bf16_f32 v87, v214, v215
	v_cvt_pk_bf16_f32 v88, v212, v213
	v_cvt_pk_bf16_f32 v89, v210, v211
	s_nop 1
	v_mfma_f32_32x32x16_bf16 v[34:49], v[82:85], v[86:89], v[34:49]
	v_lshrrev_b32_e32 v82, v163, v227
	v_bfe_i32 v83, v82, 26, 1
	v_bitop3_b32 v96, v16, s28, v83 bitop3:0xe4
	v_bfe_i32 v83, v82, 25, 1
	v_bitop3_b32 v95, v13, s28, v83 bitop3:0xe4
	v_bfe_i32 v83, v82, 24, 1
	v_bitop3_b32 v94, v14, s28, v83 bitop3:0xe4
	v_bfe_i32 v83, v82, 19, 1
	v_bitop3_b32 v93, v11, s28, v83 bitop3:0xe4
	v_bfe_i32 v83, v82, 18, 1
	v_bitop3_b32 v92, v12, s28, v83 bitop3:0xe4
	v_bfe_i32 v83, v82, 17, 1
	v_bitop3_b32 v91, v9, s28, v83 bitop3:0xe4
	v_bfe_i32 v83, v82, 16, 1
	ds_read_b128 v[226:229], v226 offset:4096
	v_bitop3_b32 v90, v10, s28, v83 bitop3:0xe4
	v_bfe_i32 v83, v82, 11, 1
	v_mfma_f32_32x32x16_bf16 v[18:33], v[98:101], v[86:89], v[18:33]
	v_bitop3_b32 v89, v7, s28, v83 bitop3:0xe4
	v_bfe_i32 v83, v82, 10, 1
	v_bitop3_b32 v88, v8, s28, v83 bitop3:0xe4
	v_bfe_i32 v83, v82, 9, 1
	v_bitop3_b32 v87, v5, s28, v83 bitop3:0xe4
	v_bfe_i32 v83, v82, 8, 1
	v_bitop3_b32 v86, v6, s28, v83 bitop3:0xe4
	v_bfe_i32 v83, v82, 3, 1
	v_bfe_i32 v84, v82, 27, 1
	v_bitop3_b32 v85, v3, s28, v83 bitop3:0xe4
	v_bfe_i32 v83, v82, 2, 1
	v_bitop3_b32 v97, v15, s28, v84 bitop3:0xe4
	v_bitop3_b32 v84, v4, s28, v83 bitop3:0xe4
	v_bfe_i32 v83, v82, 1, 1
	v_bfe_i32 v82, v82, 0, 1
	v_bitop3_b32 v83, v1, s28, v83 bitop3:0xe4
	v_bitop3_b32 v82, v2, s28, v82 bitop3:0xe4
	ds_read_b128 v[240:243], v225 offset:4096
	ds_read_b128 v[244:247], v224 offset:4096
	ds_read_b128 v[248:251], v223 offset:4096
	s_waitcnt lgkmcnt(3)
	s_nop 0
	v_mfma_f32_32x32x16_bf16 v[98:113], v[226:229], v[114:117], v[82:97]
	v_mfma_f32_32x32x16_bf16 v[82:97], v[226:229], v[130:133], v[82:97]
	s_waitcnt lgkmcnt(2)
	v_mfma_f32_32x32x16_bf16 v[98:113], v[240:243], v[118:121], v[98:113]
	v_mfma_f32_32x32x16_bf16 v[82:97], v[240:243], v[134:137], v[82:97]
	s_waitcnt lgkmcnt(1)
	v_mfma_f32_32x32x16_bf16 v[98:113], v[244:247], v[122:125], v[98:113]
	v_mfma_f32_32x32x16_bf16 v[82:97], v[244:247], v[138:141], v[82:97]
	s_waitcnt lgkmcnt(0)
	v_mfma_f32_32x32x16_bf16 v[98:113], v[248:251], v[126:129], v[98:113]
	v_mfma_f32_32x32x16_bf16 v[82:97], v[248:251], v[142:145], v[82:97]
	s_nop 10
	v_exp_f32_e32 v228, v98
	v_exp_f32_e32 v229, v99
	v_exp_f32_e32 v230, v100
	v_exp_f32_e32 v231, v101
	ds_read_b64_tr_b16 v[98:99], v179 offset:53248
	ds_read_b64_tr_b16 v[100:101], v179 offset:54272
	v_exp_f32_e32 v232, v102
	v_exp_f32_e32 v233, v103
	v_exp_f32_e32 v234, v104
	v_exp_f32_e32 v235, v105
	ds_read_b64_tr_b16 v[226:227], v179 offset:54784
	ds_read_b64_tr_b16 v[224:225], v179 offset:53760
	v_cvt_pk_bf16_f32 v102, v228, v229
	v_cvt_pk_bf16_f32 v103, v230, v231
	v_cvt_pk_bf16_f32 v104, v232, v233
	v_cvt_pk_bf16_f32 v105, v234, v235
	v_exp_f32_e32 v236, v86
	v_exp_f32_e32 v237, v87
	s_waitcnt lgkmcnt(2)
	v_mfma_f32_32x32x16_bf16 v[66:81], v[98:101], v[102:105], v[66:81]
	v_exp_f32_e32 v238, v88
	v_exp_f32_e32 v239, v89
	v_exp_f32_e32 v106, v106
	v_exp_f32_e32 v107, v107
	v_exp_f32_e32 v108, v108
	v_exp_f32_e32 v109, v109
	v_exp_f32_e32 v110, v110
	s_waitcnt lgkmcnt(0)
	v_mfma_f32_32x32x16_bf16 v[50:65], v[224:227], v[102:105], v[50:65]
	v_exp_f32_e32 v102, v82
	v_exp_f32_e32 v103, v83
	v_exp_f32_e32 v104, v84
	v_exp_f32_e32 v105, v85
	v_cvt_pk_bf16_f32 v84, v236, v237
	v_cvt_pk_bf16_f32 v82, v102, v103
	v_cvt_pk_bf16_f32 v85, v238, v239
	v_cvt_pk_bf16_f32 v83, v104, v105
	v_exp_f32_e32 v111, v111
	v_exp_f32_e32 v112, v112
	v_mfma_f32_32x32x16_bf16 v[34:49], v[98:101], v[82:85], v[34:49]
	v_exp_f32_e32 v113, v113
	v_exp_f32_e32 v90, v90
	v_exp_f32_e32 v91, v91
	v_exp_f32_e32 v92, v92
	v_exp_f32_e32 v93, v93
	v_exp_f32_e32 v94, v94
	v_exp_f32_e32 v95, v95
	v_mfma_f32_32x32x16_bf16 v[18:33], v[224:227], v[82:85], v[18:33]
	ds_read_b64_tr_b16 v[82:83], v179 offset:55296
	ds_read_b64_tr_b16 v[84:85], v179 offset:56320
	ds_read_b64_tr_b16 v[100:101], v179 offset:56832
	ds_read_b64_tr_b16 v[98:99], v179 offset:55808
	v_exp_f32_e32 v96, v96
	v_exp_f32_e32 v97, v97
	v_cvt_pk_bf16_f32 v86, v106, v107
	v_cvt_pk_bf16_f32 v87, v108, v109
	v_cvt_pk_bf16_f32 v88, v110, v111
	v_cvt_pk_bf16_f32 v89, v112, v113
	s_waitcnt lgkmcnt(2)
	s_nop 0
	v_mfma_f32_32x32x16_bf16 v[66:81], v[82:85], v[86:89], v[66:81]
	s_waitcnt lgkmcnt(0)
	v_mfma_f32_32x32x16_bf16 v[50:65], v[98:101], v[86:89], v[50:65]
	v_cvt_pk_bf16_f32 v86, v90, v91
	v_cvt_pk_bf16_f32 v87, v92, v93
	v_cvt_pk_bf16_f32 v88, v94, v95
	v_cvt_pk_bf16_f32 v89, v96, v97
	s_nop 1
	v_mfma_f32_32x32x16_bf16 v[34:49], v[82:85], v[86:89], v[34:49]
	v_add_f32_e64 v82, v190, 0
	v_add_f32_e64 v83, v191, 0
	v_add_f32_e64 v84, v228, 0
	v_add_f32_e64 v85, v229, 0
	v_add_f32_e64 v82, v192, v82
	v_add_f32_e64 v83, v193, v83
	v_pk_add_f32 v[84:85], v[230:231], v[84:85]
	v_pk_add_f32 v[82:83], v[188:189], v[82:83]
	v_pk_add_f32 v[84:85], v[232:233], v[84:85]
	v_pk_add_f32 v[82:83], v[186:187], v[82:83]
	v_mfma_f32_32x32x16_bf16 v[18:33], v[98:101], v[86:89], v[18:33]
	v_add_f32_e64 v86, v204, 0
	v_add_f32_e64 v87, v205, 0
	v_add_f32_e64 v88, v102, 0
	v_add_f32_e64 v89, v103, 0
	v_add_f32_e64 v86, v208, v86
	v_add_f32_e64 v87, v209, v87
	v_pk_add_f32 v[88:89], v[104:105], v[88:89]
	v_pk_add_f32 v[86:87], v[200:201], v[86:87]
	v_pk_add_f32 v[88:89], v[236:237], v[88:89]
	v_pk_add_f32 v[84:85], v[234:235], v[84:85]
	v_pk_add_f32 v[86:87], v[196:197], v[86:87]
	v_pk_add_f32 v[88:89], v[238:239], v[88:89]
	v_pk_add_f32 v[82:83], v[206:207], v[82:83]
	v_pk_add_f32 v[84:85], v[106:107], v[84:85]
	v_pk_add_f32 v[86:87], v[216:217], v[86:87]
	v_pk_add_f32 v[88:89], v[90:91], v[88:89]
	v_pk_add_f32 v[82:83], v[202:203], v[82:83]
	v_pk_add_f32 v[84:85], v[108:109], v[84:85]
	v_pk_add_f32 v[86:87], v[214:215], v[86:87]
	v_pk_add_f32 v[88:89], v[92:93], v[88:89]
	v_pk_add_f32 v[82:83], v[198:199], v[82:83]
	v_pk_add_f32 v[84:85], v[110:111], v[84:85]
	v_pk_add_f32 v[86:87], v[212:213], v[86:87]
	v_pk_add_f32 v[88:89], v[94:95], v[88:89]
	v_pk_add_f32 v[82:83], v[194:195], v[82:83]
	v_pk_add_f32 v[84:85], v[112:113], v[84:85]
	v_pk_add_f32 v[86:87], v[210:211], v[86:87]
	v_pk_add_f32 v[88:89], v[96:97], v[88:89]
	v_pk_add_f32 v[82:83], v[82:83], v[84:85]
	v_pk_add_f32 v[84:85], v[86:87], v[88:89]
	v_mov_b32_e32 v86, v82
	v_mov_b32_e32 v87, v84
	v_mov_b32_e32 v84, v83
	v_pk_add_f32 v[82:83], v[86:87], v[84:85]
	s_nop 0
	v_pk_add_f32 v[184:185], v[184:185], v[82:83]
	s_cbranch_scc1 .LBB0_2745
